# attn: new fast-path entry - va/EA loads first, feature barrier, then KF stream issued so loop consumes it as it arrives; Wo cvt deferred after loop; orig code kept as guard fallback
# speedup vs baseline: 1.0099x; 1.0099x over previous
_Z11attn_kernelPKfS0_PKDF16_S0_S0_S0_S2_PDF16_S3_:
	s_load_dwordx16 s[4:19], s[0:1], 0x0
	v_readfirstlane_b32 s49, v0
	s_and_b32 s22, s2, 7
	s_lshr_b32 s23, s2, 3
	s_lshl_b32 s43, s22, 1
	s_and_b32 s24, s23, 1
	s_or_b32 s33, s43, s24
	s_lshr_b32 s41, s2, 4
	s_mul_i32 s41, s41, 24
	s_lshr_b32 s51, s49, 6
	s_mul_i32 s34, s33, 0xc0
	s_mov_b32 s35, 0
	s_lshl_b32 s25, s33, 5
	s_lshl_b32 s42, s22, 5
	s_add_i32 s42, s42, s23
	s_lshl_b32 s42, s42, 10
	s_add_i32 s36, s41, 23
	s_lshr_b32 s36, s36, 4
	s_and_b32 s36, s36, 0xffffffc
	s_lshr_b32 s37, s41, 4
	s_and_b32 s37, s37, 0xffffffc
	v_lshrrev_b32_e32 v34, 5, v0
	v_bfe_u32 v35, v0, 1, 4
	v_mov_b32_e32 v115, 0
	v_lshlrev_b32_e32 v116, 4, v0
	v_and_b32_e32 v1, 63, v0
	v_add_u32_e32 v2, s41, v34
	v_lshrrev_b32_e32 v2, 1, v2
	v_mov_b32_e32 v3, v115
	v_lshl_add_u64 v[2:3], s[34:35], 0, v[2:3]
	v_lshlrev_b64 v[2:3], 9, v[2:3]
	v_lshlrev_b32_e32 v4, 5, v35
	v_mov_b32_e32 v5, v115
	v_lshrrev_b32_e32 v8, 3, v0
	v_and_b32_e32 v8, 4, v8
	v_mov_b32_e32 v9, v115
	v_and_b32_e32 v132, 0xff, v0
	v_lshl_or_b32 v132, v132, 2, s42
	v_mov_b32_e32 v133, 0
	v_cmp_gt_u32_e32 vcc, 0x100, v0
	s_movk_i32 s40, 0x200
	s_waitcnt lgkmcnt(0)
	s_add_u32 s26, s12, s25
	s_addc_u32 s27, s13, 0
	s_load_dword s52, s[26:27], s36 offset:0x0
	s_load_dword s53, s[26:27], s37 offset:0x0
	s_load_dwordx4 s[56:59], s[12:13], s25 offset:0x200
	s_load_dwordx2 s[60:61], s[12:13], s25 offset:0x210
	s_load_dwordx2 s[28:29], s[12:13], 0x400
	v_lshl_add_u64 v[2:3], s[4:5], 0, v[2:3]
	v_lshl_add_u64 v[6:7], v[2:3], 0, v[4:5]
	v_lshlrev_b32_e32 v2, 4, v35
	v_lshl_add_u64 v[10:11], v[6:7], 0, v[8:9]
	global_load_dwordx4 v[2:5], v2, s[10:11]
	s_nop 0
	global_load_dword v8, v[10:11], off offset:24
	global_load_dword v6, v[10:11], off
	global_load_dword v7, v[10:11], off offset:8
	global_load_dword v9, v[10:11], off offset:16
	v_lshl_add_u64 v[134:135], v[132:133], 2, s[14:15]
	v_mov_b32_e32 v36, s10
	v_mov_b32_e32 v37, s11
	v_cndmask_b32_e32 v134, v36, v134, vcc
	v_cndmask_b32_e32 v135, v37, v135, vcc
	s_waitcnt lgkmcnt(0)
	v_max_f32_e64 v10, s52, s52
	v_max_f32_e64 v11, s53, s53
	v_max_f32_e32 v10, v11, v10
	v_max_f32_e64 v11, s57, s57
	v_max_f32_e64 v12, s56, s56
	v_max_f32_e32 v11, v12, v11
	v_max_f32_e64 v12, s59, s59
	v_max_f32_e64 v13, s58, s58
	v_max_f32_e32 v12, v13, v12
	v_max_f32_e64 v13, s61, s61
	v_max_f32_e64 v14, s60, s60
	v_max_f32_e32 v13, v14, v13
	v_max3_f32 v11, v11, v12, v13
	s_mov_b32 s24, 0x41700000
	v_cmp_gt_f32_e32 vcc, s24, v10
	v_cmp_gt_f32_e64 s[26:27], s24, v11
	s_and_b64 s[26:27], vcc, s[26:27]
	v_cmp_lt_f32_e64 s[36:37], s29, 4.0
	s_and_b64 s[26:27], s[26:27], s[36:37]
	v_max_f32_e32 v12, v10, v10
	v_max_f32_e32 v12, 1.0, v12
	v_mul_f32_e32 v13, v12, v12
	v_mul_f32_e32 v13, v12, v13
	v_mul_f32_e32 v12, v12, v13
	v_mul_f32_e32 v12, s29, v12
	s_mov_b32 s24, 0x476a6000
	v_cmp_gt_f32_e64 s[36:37], s24, v12
	s_and_b64 s[26:27], s[26:27], s[36:37]
	s_andn2_b64 vcc, exec, s[26:27]
	s_cbranch_vccz .Lf_fast
	s_waitcnt vmcnt(0)
	s_branch .Lattn_orig
.Lf_fast:
	v_and_b32_e32 v15, 1, v0
	v_cmp_eq_u32_e32 vcc, 0, v15
	s_waitcnt vmcnt(4)
	v_mov_b32_e32 v10, v2
	v_mov_b32_e32 v11, v4
	v_mov_b32_e32 v12, v3
	v_cndmask_b32_e32 v13, 0, v5, vcc
	s_waitcnt vmcnt(3)
	v_cndmask_b32_e64 v14, v8, 1.0, vcc
	v_pk_add_f32 v[10:11], v[10:11], v[12:13]
	s_waitcnt vmcnt(1)
	v_pk_mul_f32 v[12:13], v[6:7], v[14:15] op_sel_hi:[1,0]
	v_pk_add_f32 v[10:11], v[10:11], v[10:11] op_sel:[0,1] op_sel_hi:[1,0]
	v_mov_b32_e32 v8, v6
	v_mov_b32_e32 v16, v13
	v_pk_add_f32 v[22:23], v[10:11], v[2:3] op_sel_hi:[0,1] neg_lo:[0,1] neg_hi:[0,1]
	v_mov_b32_e32 v17, v14
	s_waitcnt vmcnt(0)
	v_pk_mul_f32 v[8:9], v[8:9], v[16:17]
	v_mov_b32_e32 v16, v22
	v_mov_b32_e32 v17, v10
	v_mov_b32_e32 v2, v3
	v_mov_b32_e32 v3, v4
	v_fma_mixlo_f16 v5, v14, v10, 0
	v_pk_add_f32 v[10:11], v[16:17], v[2:3] neg_lo:[0,1] neg_hi:[0,1]
	v_pk_mul_f32 v[2:3], v[12:13], v[22:23]
	v_pk_add_f32 v[16:17], v[22:23], v[4:5] op_sel_hi:[1,0] neg_lo:[0,1] neg_hi:[0,1]
	v_cvt_pk_f16_f32 v3, v2, v3
	v_sub_f32_e32 v22, v10, v4
	v_pack_b32_f16 v2, v5, v3
	v_pk_mul_f32 v[4:5], v[8:9], v[10:11]
	v_pk_mul_f32 v[10:11], v[6:7], v[8:9] op_sel:[0,1]
	v_cvt_pk_f16_f32 v23, v4, v5
	v_pk_mul_f32 v[4:5], v[10:11], v[16:17]
	v_lshlrev_b32_e32 v7, 7, v35
	v_cvt_pk_f16_f32 v5, v4, v5
	v_lshlrev_b32_e32 v15, 5, v15
	v_mul_f32_e32 v6, v6, v11
	v_alignbit_b32 v4, v5, v23, 16
	v_lshrrev_b32_e32 v5, 16, v5
	v_or3_b32 v7, v7, v15, v34
	v_alignbit_b32 v3, v23, v3, 16
	v_fma_mixhi_f16 v5, v6, v22, 0
	v_lshl_add_u32 v7, v7, 4, 0
	ds_write_b128 v7, v[2:5]
	v_cvt_pk_f16_f32 v2, v14, v12
	v_cvt_pk_f16_f32 v3, v13, v8
	v_cvt_pk_f16_f32 v4, v9, v10
	v_cvt_pk_f16_f32 v5, v11, v6
	v_cmp_gt_u32_e32 vcc, s40, v0
	ds_write_b128 v7, v[2:5] offset:1024
	s_and_saveexec_b64 s[2:3], vcc
	s_cbranch_execz .Lf_27
	v_lshlrev_b32_e32 v2, 2, v0
	v_and_b32_e32 v3, 7, v0
	s_movk_i32 s4, 0x7e0
	v_and_or_b32 v2, v2, s4, v3
	v_lshl_add_u32 v2, v2, 4, 0
	v_mov_b32_e32 v4, v115
	v_mov_b32_e32 v5, v115
	v_mov_b32_e32 v6, v115
	v_mov_b32_e32 v7, v115
	ds_write_b128 v2, v[4:7] offset:384
.Lf_27:
	s_or_b64 exec, exec, s[2:3]
	v_and_b32_e32 v2, 0x3f0, v116
	v_add_u32_e32 v136, 0, v2
	s_waitcnt lgkmcnt(0)
	s_barrier
	v_and_b32_e32 v10, 31, v0
	s_mul_i32 s38, s33, 0x1800
	s_mov_b32 s39, 0
	v_lshl_or_b32 v114, s51, 5, v10
	v_lshl_add_u64 v[12:13], s[38:39], 0, v[114:115]
	v_lshrrev_b32_e32 v1, 5, v1
	v_lshlrev_b64 v[12:13], 5, v[12:13]
	v_lshlrev_b32_e32 v10, 4, v1
	v_mov_b32_e32 v11, v115
	v_lshl_add_u64 v[12:13], s[16:17], 0, v[12:13]
	s_movk_i32 s6, 0x3000
	v_lshl_add_u64 v[10:11], v[12:13], 0, v[10:11]
	v_add_co_u32_e32 v12, vcc, s6, v10
	s_movk_i32 s7, 0x6000
	s_nop 0
	v_addc_co_u32_e32 v13, vcc, 0, v11, vcc
	v_add_co_u32_e32 v14, vcc, s7, v10
	s_mov_b32 s8, 0x9000
	s_nop 0
	v_addc_co_u32_e32 v15, vcc, 0, v11, vcc
	v_add_co_u32_e32 v16, vcc, s8, v10
	s_mov_b32 s9, 0xc000
	s_nop 0
	v_addc_co_u32_e32 v17, vcc, 0, v11, vcc
	v_add_co_u32_e32 v22, vcc, s9, v10
	s_mov_b32 s10, 0xf000
	s_nop 0
	v_addc_co_u32_e32 v23, vcc, 0, v11, vcc
	v_add_co_u32_e32 v24, vcc, s10, v10
	s_mov_b32 s11, 0x12000
	s_nop 0
	v_addc_co_u32_e32 v25, vcc, 0, v11, vcc
	v_add_co_u32_e32 v26, vcc, s11, v10
	s_mov_b32 s12, 0x15000
	s_nop 0
	v_addc_co_u32_e32 v27, vcc, 0, v11, vcc
	v_add_co_u32_e32 v28, vcc, s12, v10
	s_mov_b32 s13, 0x18000
	s_nop 0
	v_addc_co_u32_e32 v29, vcc, 0, v11, vcc
	global_load_dwordx4 v[18:21], v[10:11], off
	global_load_dwordx4 v[30:33], v[12:13], off
	global_load_dwordx4 v[110:113], v[14:15], off
	global_load_dwordx4 v[106:109], v[16:17], off
	global_load_dwordx4 v[102:105], v[22:23], off
	global_load_dwordx4 v[98:101], v[24:25], off
	global_load_dwordx4 v[94:97], v[26:27], off
	global_load_dwordx4 v[90:93], v[28:29], off
	v_add_co_u32_e32 v12, vcc, s13, v10
	s_mov_b32 s40, 0x1b000
	s_nop 0
	v_addc_co_u32_e32 v13, vcc, 0, v11, vcc
	v_add_co_u32_e32 v14, vcc, s40, v10
	s_mov_b32 s40, 0x1e000
	s_nop 0
	v_addc_co_u32_e32 v15, vcc, 0, v11, vcc
	global_load_dwordx4 v[86:89], v[12:13], off
	global_load_dwordx4 v[82:85], v[14:15], off
	v_add_co_u32_e32 v12, vcc, s40, v10
	s_mov_b32 s40, 0x21000
	s_nop 0
	v_addc_co_u32_e32 v13, vcc, 0, v11, vcc
	v_add_co_u32_e32 v14, vcc, s40, v10
	s_mov_b32 s40, 0x24000
	s_nop 0
	v_addc_co_u32_e32 v15, vcc, 0, v11, vcc
	v_add_co_u32_e32 v16, vcc, s40, v10
	s_mov_b32 s40, 0x27000
	s_nop 0
	v_addc_co_u32_e32 v17, vcc, 0, v11, vcc
	v_add_co_u32_e32 v22, vcc, s40, v10
	s_mov_b32 s40, 0x2a000
	s_nop 0
	v_addc_co_u32_e32 v23, vcc, 0, v11, vcc
	v_add_co_u32_e32 v24, vcc, s40, v10
	s_mov_b32 s40, 0x2d000
	s_nop 0
	v_addc_co_u32_e32 v25, vcc, 0, v11, vcc
	v_add_co_u32_e32 v10, vcc, s40, v10
	s_movk_i32 s40, 0x200
	s_nop 0
	v_addc_co_u32_e32 v11, vcc, 0, v11, vcc
	global_load_dwordx4 v[78:81], v[12:13], off
	global_load_dwordx4 v[74:77], v[14:15], off
	global_load_dwordx4 v[70:73], v[16:17], off
	global_load_dwordx4 v[66:69], v[22:23], off
	global_load_dwordx4 v[62:65], v[24:25], off
	global_load_dwordx4 v[58:61], v[10:11], off
	global_load_dwordx4 v[128:131], v[134:135], off
	ds_read_b128 v[2:5], v136
	ds_read_b128 v[22:25], v136 offset:1024
	ds_read_b128 v[34:37], v136 offset:2048
	ds_read_b128 v[38:41], v136 offset:3072
	s_waitcnt vmcnt(16) lgkmcnt(3)
	v_mfma_f32_32x32x16_f16 v[2:17], v[2:5], v[18:21], 0
	s_add_i32 s2, 0, 0x18000
	v_mul_u32_u24_e32 v1, 0xc40, v1
	s_waitcnt lgkmcnt(2)
	v_mfma_f32_32x32x16_f16 v[14:29], v[22:25], v[18:21], 0
	s_waitcnt vmcnt(15) lgkmcnt(1)
	v_mfma_f32_32x32x16_f16 v[42:57], v[34:37], v[30:33], 0
	s_waitcnt lgkmcnt(0)
	v_mfma_f32_32x32x16_f16 v[26:41], v[38:41], v[30:33], 0
	s_nop 9
	v_mul_f32_e64 v42, v42, v14
	v_mul_f32_e64 v43, v43, v15
	v_pk_mul_f32 v[14:15], v[14:15], v[26:27]
	v_pk_mul_f32 v[38:39], v[44:45], v[16:17]
	v_rcp_f32_e32 v14, v14
	v_rcp_f32_e32 v15, v15
	v_pk_fma_f32 v[2:3], v[2:3], v[26:27], v[42:43]
	v_pk_mul_f32 v[16:17], v[16:17], v[28:29]
	v_pk_mul_f32 v[40:41], v[46:47], v[18:19]
	v_pk_fma_f32 v[116:117], v[2:3], v[14:15], 0 op_sel_hi:[1,1,0]
	v_rcp_f32_e32 v2, v16
	v_rcp_f32_e32 v3, v17
	v_pk_fma_f32 v[4:5], v[4:5], v[28:29], v[38:39]
	v_pk_mul_f32 v[18:19], v[18:19], v[30:31]
	v_pk_mul_f32 v[44:45], v[48:49], v[20:21]
	v_pk_fma_f32 v[118:119], v[4:5], v[2:3], 0 op_sel_hi:[1,1,0]
	v_rcp_f32_e32 v2, v18
	v_rcp_f32_e32 v3, v19
	v_pk_fma_f32 v[6:7], v[6:7], v[30:31], v[40:41]
	v_pk_mul_f32 v[20:21], v[20:21], v[32:33]
	v_pk_mul_f32 v[46:47], v[50:51], v[22:23]
	v_pk_fma_f32 v[120:121], v[6:7], v[2:3], 0 op_sel_hi:[1,1,0]
	v_rcp_f32_e32 v2, v20
	v_rcp_f32_e32 v3, v21
	v_pk_fma_f32 v[8:9], v[8:9], v[32:33], v[44:45]
	v_pk_mul_f32 v[22:23], v[22:23], v[34:35]
	v_pk_mul_f32 v[48:49], v[52:53], v[24:25]
	v_pk_fma_f32 v[122:123], v[8:9], v[2:3], 0 op_sel_hi:[1,1,0]
	v_rcp_f32_e32 v2, v22
	v_rcp_f32_e32 v3, v23
	v_pk_fma_f32 v[10:11], v[10:11], v[34:35], v[46:47]
	v_pk_mul_f32 v[24:25], v[24:25], v[36:37]
	v_pk_fma_f32 v[12:13], v[12:13], v[36:37], v[48:49]
	v_pk_fma_f32 v[124:125], v[10:11], v[2:3], 0 op_sel_hi:[1,1,0]
	v_rcp_f32_e32 v2, v24
	v_rcp_f32_e32 v3, v25
	s_nop 0
	v_pk_fma_f32 v[126:127], v[12:13], v[2:3], 0 op_sel_hi:[1,1,0]
	ds_read_b128 v[2:5], v136 offset:4096
	ds_read_b128 v[18:21], v136 offset:5120
	ds_read_b128 v[30:33], v136 offset:6144
	ds_read_b128 v[34:37], v136 offset:7168
	s_waitcnt vmcnt(14) lgkmcnt(3)
	v_mfma_f32_32x32x16_f16 v[2:17], v[2:5], v[110:113], 0
	s_waitcnt lgkmcnt(2)
	v_mfma_f32_32x32x16_f16 v[14:29], v[18:21], v[110:113], 0
	s_waitcnt vmcnt(13) lgkmcnt(1)
	v_mfma_f32_32x32x16_f16 v[42:57], v[30:33], v[106:109], 0
	s_waitcnt lgkmcnt(0)
	v_mfma_f32_32x32x16_f16 v[26:41], v[34:37], v[106:109], 0
	s_nop 9
	v_mul_f32_e64 v42, v42, v14
	v_mul_f32_e64 v43, v43, v15
	v_pk_mul_f32 v[14:15], v[14:15], v[26:27]
	v_pk_mul_f32 v[38:39], v[44:45], v[16:17]
	v_rcp_f32_e32 v14, v14
	v_rcp_f32_e32 v15, v15
	v_pk_fma_f32 v[2:3], v[2:3], v[26:27], v[42:43]
	v_pk_mul_f32 v[16:17], v[16:17], v[28:29]
	v_pk_mul_f32 v[40:41], v[46:47], v[18:19]
	v_pk_fma_f32 v[106:107], v[2:3], v[14:15], v[116:117]
	v_rcp_f32_e32 v2, v16
	v_rcp_f32_e32 v3, v17
	v_pk_fma_f32 v[4:5], v[4:5], v[28:29], v[38:39]
	v_pk_mul_f32 v[18:19], v[18:19], v[30:31]
	v_pk_mul_f32 v[44:45], v[48:49], v[20:21]
	v_pk_fma_f32 v[108:109], v[4:5], v[2:3], v[118:119]
	v_rcp_f32_e32 v2, v18
	v_rcp_f32_e32 v3, v19
	v_pk_fma_f32 v[6:7], v[6:7], v[30:31], v[40:41]
	v_pk_mul_f32 v[20:21], v[20:21], v[32:33]
	v_pk_mul_f32 v[46:47], v[50:51], v[22:23]
	v_pk_fma_f32 v[110:111], v[6:7], v[2:3], v[120:121]
	v_rcp_f32_e32 v2, v20
	v_rcp_f32_e32 v3, v21
	v_pk_fma_f32 v[8:9], v[8:9], v[32:33], v[44:45]
	v_pk_mul_f32 v[22:23], v[22:23], v[34:35]
	v_pk_mul_f32 v[48:49], v[52:53], v[24:25]
	v_pk_fma_f32 v[112:113], v[8:9], v[2:3], v[122:123]
	v_rcp_f32_e32 v2, v22
	v_rcp_f32_e32 v3, v23
	v_pk_fma_f32 v[10:11], v[10:11], v[34:35], v[46:47]
	v_pk_mul_f32 v[24:25], v[24:25], v[36:37]
	v_pk_fma_f32 v[12:13], v[12:13], v[36:37], v[48:49]
	v_pk_fma_f32 v[116:117], v[10:11], v[2:3], v[124:125]
	v_rcp_f32_e32 v2, v24
	v_rcp_f32_e32 v3, v25
	s_nop 0
	v_pk_fma_f32 v[118:119], v[12:13], v[2:3], v[126:127]
	ds_read_b128 v[2:5], v136 offset:8192
	ds_read_b128 v[18:21], v136 offset:9216
	ds_read_b128 v[30:33], v136 offset:10240
	ds_read_b128 v[34:37], v136 offset:11264
	s_waitcnt vmcnt(12) lgkmcnt(3)
	v_mfma_f32_32x32x16_f16 v[2:17], v[2:5], v[102:105], 0
	s_waitcnt lgkmcnt(2)
	v_mfma_f32_32x32x16_f16 v[14:29], v[18:21], v[102:105], 0
	s_waitcnt vmcnt(11) lgkmcnt(1)
	v_mfma_f32_32x32x16_f16 v[42:57], v[30:33], v[98:101], 0
	s_waitcnt lgkmcnt(0)
	v_mfma_f32_32x32x16_f16 v[26:41], v[34:37], v[98:101], 0
	s_nop 9
	v_mul_f32_e64 v42, v42, v14
	v_mul_f32_e64 v43, v43, v15
	v_pk_mul_f32 v[14:15], v[14:15], v[26:27]
	v_pk_mul_f32 v[38:39], v[44:45], v[16:17]
	v_rcp_f32_e32 v14, v14
	v_rcp_f32_e32 v15, v15
	v_pk_fma_f32 v[2:3], v[2:3], v[26:27], v[42:43]
	v_pk_mul_f32 v[16:17], v[16:17], v[28:29]
	v_pk_mul_f32 v[40:41], v[46:47], v[18:19]
	v_pk_fma_f32 v[98:99], v[2:3], v[14:15], v[106:107]
	v_rcp_f32_e32 v2, v16
	v_rcp_f32_e32 v3, v17
	v_pk_fma_f32 v[4:5], v[4:5], v[28:29], v[38:39]
	v_pk_mul_f32 v[18:19], v[18:19], v[30:31]
	v_pk_mul_f32 v[44:45], v[48:49], v[20:21]
	v_pk_fma_f32 v[100:101], v[4:5], v[2:3], v[108:109]
	v_rcp_f32_e32 v2, v18
	v_rcp_f32_e32 v3, v19
	v_pk_fma_f32 v[6:7], v[6:7], v[30:31], v[40:41]
	v_pk_mul_f32 v[20:21], v[20:21], v[32:33]
	v_pk_mul_f32 v[46:47], v[50:51], v[22:23]
	v_pk_fma_f32 v[102:103], v[6:7], v[2:3], v[110:111]
	v_rcp_f32_e32 v2, v20
	v_rcp_f32_e32 v3, v21
	v_pk_fma_f32 v[8:9], v[8:9], v[32:33], v[44:45]
	v_pk_mul_f32 v[22:23], v[22:23], v[34:35]
	v_pk_mul_f32 v[48:49], v[52:53], v[24:25]
	v_pk_fma_f32 v[104:105], v[8:9], v[2:3], v[112:113]
	v_rcp_f32_e32 v2, v22
	v_rcp_f32_e32 v3, v23
	v_pk_fma_f32 v[10:11], v[10:11], v[34:35], v[46:47]
	v_pk_mul_f32 v[24:25], v[24:25], v[36:37]
	v_pk_fma_f32 v[12:13], v[12:13], v[36:37], v[48:49]
	v_pk_fma_f32 v[106:107], v[10:11], v[2:3], v[116:117]
	v_rcp_f32_e32 v2, v24
	v_rcp_f32_e32 v3, v25
	s_nop 0
	v_pk_fma_f32 v[108:109], v[12:13], v[2:3], v[118:119]
	ds_read_b128 v[2:5], v136 offset:12288
	ds_read_b128 v[18:21], v136 offset:13312
	ds_read_b128 v[30:33], v136 offset:14336
	ds_read_b128 v[34:37], v136 offset:15360
	s_waitcnt vmcnt(10) lgkmcnt(3)
	v_mfma_f32_32x32x16_f16 v[2:17], v[2:5], v[94:97], 0
	s_waitcnt lgkmcnt(2)
	v_mfma_f32_32x32x16_f16 v[14:29], v[18:21], v[94:97], 0
	s_waitcnt vmcnt(9) lgkmcnt(1)
	v_mfma_f32_32x32x16_f16 v[42:57], v[30:33], v[90:93], 0
	s_waitcnt lgkmcnt(0)
	v_mfma_f32_32x32x16_f16 v[26:41], v[34:37], v[90:93], 0
	s_nop 9
	v_mul_f32_e64 v42, v42, v14
	v_mul_f32_e64 v43, v43, v15
	v_pk_mul_f32 v[14:15], v[14:15], v[26:27]
	v_pk_mul_f32 v[38:39], v[44:45], v[16:17]
	v_rcp_f32_e32 v14, v14
	v_rcp_f32_e32 v15, v15
	v_pk_fma_f32 v[2:3], v[2:3], v[26:27], v[42:43]
	v_pk_mul_f32 v[16:17], v[16:17], v[28:29]
	v_pk_mul_f32 v[40:41], v[46:47], v[18:19]
	v_pk_fma_f32 v[90:91], v[2:3], v[14:15], v[98:99]
	v_rcp_f32_e32 v2, v16
	v_rcp_f32_e32 v3, v17
	v_pk_fma_f32 v[4:5], v[4:5], v[28:29], v[38:39]
	v_pk_mul_f32 v[18:19], v[18:19], v[30:31]
	v_pk_mul_f32 v[44:45], v[48:49], v[20:21]
	v_pk_fma_f32 v[92:93], v[4:5], v[2:3], v[100:101]
	v_rcp_f32_e32 v2, v18
	v_rcp_f32_e32 v3, v19
	v_pk_fma_f32 v[6:7], v[6:7], v[30:31], v[40:41]
	v_pk_mul_f32 v[20:21], v[20:21], v[32:33]
	v_pk_mul_f32 v[46:47], v[50:51], v[22:23]
	v_pk_fma_f32 v[94:95], v[6:7], v[2:3], v[102:103]
	v_rcp_f32_e32 v2, v20
	v_rcp_f32_e32 v3, v21
	v_pk_fma_f32 v[8:9], v[8:9], v[32:33], v[44:45]
	v_pk_mul_f32 v[22:23], v[22:23], v[34:35]
	v_pk_mul_f32 v[48:49], v[52:53], v[24:25]
	v_pk_fma_f32 v[96:97], v[8:9], v[2:3], v[104:105]
	v_rcp_f32_e32 v2, v22
	v_rcp_f32_e32 v3, v23
	v_pk_fma_f32 v[10:11], v[10:11], v[34:35], v[46:47]
	v_pk_mul_f32 v[24:25], v[24:25], v[36:37]
	v_pk_fma_f32 v[12:13], v[12:13], v[36:37], v[48:49]
	v_pk_fma_f32 v[98:99], v[10:11], v[2:3], v[106:107]
	v_rcp_f32_e32 v2, v24
	v_rcp_f32_e32 v3, v25
	s_nop 0
	v_pk_fma_f32 v[100:101], v[12:13], v[2:3], v[108:109]
	ds_read_b128 v[2:5], v136 offset:16384
	ds_read_b128 v[18:21], v136 offset:17408
	ds_read_b128 v[30:33], v136 offset:18432
	ds_read_b128 v[34:37], v136 offset:19456
	s_waitcnt vmcnt(8) lgkmcnt(3)
	v_mfma_f32_32x32x16_f16 v[2:17], v[2:5], v[86:89], 0
	s_waitcnt lgkmcnt(2)
	v_mfma_f32_32x32x16_f16 v[14:29], v[18:21], v[86:89], 0
	s_waitcnt vmcnt(7) lgkmcnt(1)
	v_mfma_f32_32x32x16_f16 v[42:57], v[30:33], v[82:85], 0
	s_waitcnt lgkmcnt(0)
	v_mfma_f32_32x32x16_f16 v[26:41], v[34:37], v[82:85], 0
	s_nop 9
	v_mul_f32_e64 v42, v42, v14
	v_mul_f32_e64 v43, v43, v15
	v_pk_mul_f32 v[14:15], v[14:15], v[26:27]
	v_pk_mul_f32 v[38:39], v[44:45], v[16:17]
	v_rcp_f32_e32 v14, v14
	v_rcp_f32_e32 v15, v15
	v_pk_fma_f32 v[2:3], v[2:3], v[26:27], v[42:43]
	v_pk_mul_f32 v[16:17], v[16:17], v[28:29]
	v_pk_mul_f32 v[40:41], v[46:47], v[18:19]
	v_pk_fma_f32 v[82:83], v[2:3], v[14:15], v[90:91]
	v_rcp_f32_e32 v2, v16
	v_rcp_f32_e32 v3, v17
	v_pk_fma_f32 v[4:5], v[4:5], v[28:29], v[38:39]
	v_pk_mul_f32 v[18:19], v[18:19], v[30:31]
	v_pk_mul_f32 v[44:45], v[48:49], v[20:21]
	v_pk_fma_f32 v[84:85], v[4:5], v[2:3], v[92:93]
	v_rcp_f32_e32 v2, v18
	v_rcp_f32_e32 v3, v19
	v_pk_fma_f32 v[6:7], v[6:7], v[30:31], v[40:41]
	v_pk_mul_f32 v[20:21], v[20:21], v[32:33]
	v_pk_mul_f32 v[46:47], v[50:51], v[22:23]
	v_pk_fma_f32 v[86:87], v[6:7], v[2:3], v[94:95]
	v_rcp_f32_e32 v2, v20
	v_rcp_f32_e32 v3, v21
	v_pk_fma_f32 v[8:9], v[8:9], v[32:33], v[44:45]
	v_pk_mul_f32 v[22:23], v[22:23], v[34:35]
	v_pk_mul_f32 v[48:49], v[52:53], v[24:25]
	v_pk_fma_f32 v[88:89], v[8:9], v[2:3], v[96:97]
	v_rcp_f32_e32 v2, v22
	v_rcp_f32_e32 v3, v23
	v_pk_fma_f32 v[10:11], v[10:11], v[34:35], v[46:47]
	v_pk_mul_f32 v[24:25], v[24:25], v[36:37]
	v_pk_fma_f32 v[12:13], v[12:13], v[36:37], v[48:49]
	v_pk_fma_f32 v[90:91], v[10:11], v[2:3], v[98:99]
	v_rcp_f32_e32 v2, v24
	v_rcp_f32_e32 v3, v25
	s_nop 0
	v_pk_fma_f32 v[92:93], v[12:13], v[2:3], v[100:101]
	ds_read_b128 v[2:5], v136 offset:20480
	ds_read_b128 v[18:21], v136 offset:21504
	ds_read_b128 v[30:33], v136 offset:22528
	ds_read_b128 v[34:37], v136 offset:23552
	s_waitcnt vmcnt(6) lgkmcnt(3)
	v_mfma_f32_32x32x16_f16 v[2:17], v[2:5], v[78:81], 0
	s_waitcnt lgkmcnt(2)
	v_mfma_f32_32x32x16_f16 v[14:29], v[18:21], v[78:81], 0
	s_waitcnt vmcnt(5) lgkmcnt(1)
	v_mfma_f32_32x32x16_f16 v[42:57], v[30:33], v[74:77], 0
	s_waitcnt lgkmcnt(0)
	v_mfma_f32_32x32x16_f16 v[26:41], v[34:37], v[74:77], 0
	s_nop 9
	v_mul_f32_e64 v42, v42, v14
	v_mul_f32_e64 v43, v43, v15
	v_pk_mul_f32 v[14:15], v[14:15], v[26:27]
	v_pk_mul_f32 v[38:39], v[44:45], v[16:17]
	v_rcp_f32_e32 v14, v14
	v_rcp_f32_e32 v15, v15
	v_pk_fma_f32 v[2:3], v[2:3], v[26:27], v[42:43]
	v_pk_mul_f32 v[16:17], v[16:17], v[28:29]
	v_pk_mul_f32 v[40:41], v[46:47], v[18:19]
	v_pk_fma_f32 v[74:75], v[2:3], v[14:15], v[82:83]
	v_rcp_f32_e32 v2, v16
	v_rcp_f32_e32 v3, v17
	v_pk_fma_f32 v[4:5], v[4:5], v[28:29], v[38:39]
	v_pk_mul_f32 v[18:19], v[18:19], v[30:31]
	v_pk_mul_f32 v[44:45], v[48:49], v[20:21]
	v_pk_fma_f32 v[76:77], v[4:5], v[2:3], v[84:85]
	v_rcp_f32_e32 v2, v18
	v_rcp_f32_e32 v3, v19
	v_pk_fma_f32 v[6:7], v[6:7], v[30:31], v[40:41]
	v_pk_mul_f32 v[20:21], v[20:21], v[32:33]
	v_pk_mul_f32 v[46:47], v[50:51], v[22:23]
	v_pk_fma_f32 v[78:79], v[6:7], v[2:3], v[86:87]
	v_rcp_f32_e32 v2, v20
	v_rcp_f32_e32 v3, v21
	v_pk_fma_f32 v[8:9], v[8:9], v[32:33], v[44:45]
	v_pk_mul_f32 v[22:23], v[22:23], v[34:35]
	v_pk_mul_f32 v[48:49], v[52:53], v[24:25]
	v_pk_fma_f32 v[80:81], v[8:9], v[2:3], v[88:89]
	v_rcp_f32_e32 v2, v22
	v_rcp_f32_e32 v3, v23
	v_pk_fma_f32 v[10:11], v[10:11], v[34:35], v[46:47]
	v_pk_mul_f32 v[24:25], v[24:25], v[36:37]
	v_pk_fma_f32 v[12:13], v[12:13], v[36:37], v[48:49]
	v_pk_fma_f32 v[82:83], v[10:11], v[2:3], v[90:91]
	v_rcp_f32_e32 v2, v24
	v_rcp_f32_e32 v3, v25
	s_nop 0
	v_pk_fma_f32 v[84:85], v[12:13], v[2:3], v[92:93]
	ds_read_b128 v[2:5], v136 offset:24576
	ds_read_b128 v[18:21], v136 offset:25600
	ds_read_b128 v[30:33], v136 offset:26624
	ds_read_b128 v[34:37], v136 offset:27648
	s_waitcnt vmcnt(4) lgkmcnt(3)
	v_mfma_f32_32x32x16_f16 v[2:17], v[2:5], v[70:73], 0
	s_waitcnt lgkmcnt(2)
	v_mfma_f32_32x32x16_f16 v[14:29], v[18:21], v[70:73], 0
	s_waitcnt vmcnt(3) lgkmcnt(1)
	v_mfma_f32_32x32x16_f16 v[42:57], v[30:33], v[66:69], 0
	s_waitcnt lgkmcnt(0)
	v_mfma_f32_32x32x16_f16 v[26:41], v[34:37], v[66:69], 0
	s_nop 9
	v_mul_f32_e64 v42, v42, v14
	v_mul_f32_e64 v43, v43, v15
	v_pk_mul_f32 v[14:15], v[14:15], v[26:27]
	v_pk_mul_f32 v[38:39], v[44:45], v[16:17]
	v_rcp_f32_e32 v14, v14
	v_rcp_f32_e32 v15, v15
	v_pk_fma_f32 v[2:3], v[2:3], v[26:27], v[42:43]
	v_pk_mul_f32 v[16:17], v[16:17], v[28:29]
	v_pk_mul_f32 v[40:41], v[46:47], v[18:19]
	v_pk_fma_f32 v[74:75], v[2:3], v[14:15], v[74:75]
	v_rcp_f32_e32 v2, v16
	v_rcp_f32_e32 v3, v17
	v_pk_fma_f32 v[4:5], v[4:5], v[28:29], v[38:39]
	v_pk_mul_f32 v[18:19], v[18:19], v[30:31]
	v_pk_mul_f32 v[44:45], v[48:49], v[20:21]
	v_pk_fma_f32 v[76:77], v[4:5], v[2:3], v[76:77]
	v_rcp_f32_e32 v2, v18
	v_rcp_f32_e32 v3, v19
	v_pk_fma_f32 v[6:7], v[6:7], v[30:31], v[40:41]
	v_pk_mul_f32 v[20:21], v[20:21], v[32:33]
	v_pk_mul_f32 v[46:47], v[50:51], v[22:23]
	v_pk_fma_f32 v[72:73], v[6:7], v[2:3], v[78:79]
	v_rcp_f32_e32 v2, v20
	v_rcp_f32_e32 v3, v21
	v_pk_fma_f32 v[8:9], v[8:9], v[32:33], v[44:45]
	v_pk_mul_f32 v[22:23], v[22:23], v[34:35]
	v_pk_mul_f32 v[48:49], v[52:53], v[24:25]
	v_pk_fma_f32 v[70:71], v[8:9], v[2:3], v[80:81]
	v_rcp_f32_e32 v2, v22
	v_rcp_f32_e32 v3, v23
	v_pk_fma_f32 v[10:11], v[10:11], v[34:35], v[46:47]
	v_pk_mul_f32 v[24:25], v[24:25], v[36:37]
	v_pk_fma_f32 v[12:13], v[12:13], v[36:37], v[48:49]
	v_pk_fma_f32 v[66:67], v[10:11], v[2:3], v[82:83]
	v_rcp_f32_e32 v2, v24
	v_rcp_f32_e32 v3, v25
	s_nop 0
	v_pk_fma_f32 v[68:69], v[12:13], v[2:3], v[84:85]
	ds_read_b128 v[2:5], v136 offset:28672
	ds_read_b128 v[18:21], v136 offset:29696
	ds_read_b128 v[30:33], v136 offset:30720
	ds_read_b128 v[34:37], v136 offset:31744
	s_waitcnt vmcnt(2) lgkmcnt(3)
	v_mfma_f32_32x32x16_f16 v[2:17], v[2:5], v[62:65], 0
	s_waitcnt lgkmcnt(2)
	v_mfma_f32_32x32x16_f16 v[14:29], v[18:21], v[62:65], 0
	s_waitcnt vmcnt(1) lgkmcnt(1)
	v_mfma_f32_32x32x16_f16 v[42:57], v[30:33], v[58:61], 0
	s_waitcnt lgkmcnt(0)
	v_mfma_f32_32x32x16_f16 v[26:41], v[34:37], v[58:61], 0
	s_nop 9
	v_mul_f32_e64 v42, v42, v14
	v_mul_f32_e64 v43, v43, v15
	v_pk_mul_f32 v[14:15], v[14:15], v[26:27]
	v_pk_mul_f32 v[38:39], v[44:45], v[16:17]
	v_rcp_f32_e32 v14, v14
	v_rcp_f32_e32 v15, v15
	v_pk_fma_f32 v[2:3], v[2:3], v[26:27], v[42:43]
	v_pk_mul_f32 v[16:17], v[16:17], v[28:29]
	v_pk_mul_f32 v[40:41], v[46:47], v[18:19]
	v_pk_fma_f32 v[14:15], v[2:3], v[14:15], v[74:75]
	v_rcp_f32_e32 v2, v16
	v_rcp_f32_e32 v3, v17
	v_pk_fma_f32 v[4:5], v[4:5], v[28:29], v[38:39]
	v_pk_mul_f32 v[18:19], v[18:19], v[30:31]
	v_pk_mul_f32 v[44:45], v[48:49], v[20:21]
	v_pk_fma_f32 v[4:5], v[4:5], v[2:3], v[76:77]
	v_rcp_f32_e32 v2, v18
	v_rcp_f32_e32 v3, v19
	v_pk_fma_f32 v[6:7], v[6:7], v[30:31], v[40:41]
	v_pk_mul_f32 v[20:21], v[20:21], v[32:33]
	v_pk_mul_f32 v[46:47], v[50:51], v[22:23]
	v_pk_fma_f32 v[6:7], v[6:7], v[2:3], v[72:73]
	v_rcp_f32_e32 v2, v20
	v_rcp_f32_e32 v3, v21
	v_pk_fma_f32 v[8:9], v[8:9], v[32:33], v[44:45]
	v_pk_mul_f32 v[22:23], v[22:23], v[34:35]
	v_fma_f32 v4, v4, -2.0, s28
	v_pk_fma_f32 v[8:9], v[8:9], v[2:3], v[70:71]
	v_rcp_f32_e32 v2, v22
	v_rcp_f32_e32 v3, v23
	v_subrev_f32_e32 v4, s29, v4
	v_mul_f32_e32 v4, 0x3fb8aa3b, v4
	v_exp_f32_e32 v4, v4
	v_pk_mul_f32 v[48:49], v[52:53], v[24:25]
	v_pk_fma_f32 v[10:11], v[10:11], v[34:35], v[46:47]
	v_pk_mul_f32 v[24:25], v[24:25], v[36:37]
	v_pk_fma_f32 v[10:11], v[10:11], v[2:3], v[66:67]
	v_rcp_f32_e32 v2, v24
	v_rcp_f32_e32 v3, v25
	v_cvt_f16_f32_e32 v4, v4
	v_pk_fma_f32 v[12:13], v[12:13], v[36:37], v[48:49]
	s_nop 0
	v_pk_fma_f32 v[2:3], v[12:13], v[2:3], v[68:69]
	v_lshlrev_b32_e32 v12, 1, v114
	v_add3_u32 v1, s2, v12, v1
	ds_write_b16 v1, v4 offset:1568
	v_fma_f32 v4, v5, -2.0, s28
	v_subrev_f32_e32 v4, s29, v4
	v_mul_f32_e32 v4, 0x3fb8aa3b, v4
	v_exp_f32_e32 v4, v4
	v_fma_f32 v2, v2, -2.0, s28
	v_subrev_f32_e32 v2, s29, v2
	v_mul_f32_e32 v2, 0x3fb8aa3b, v2
	v_cvt_f16_f32_e32 v4, v4
	v_exp_f32_e32 v2, v2
	v_fma_f32 v13, v14, -2.0, s28
	v_fma_f32 v12, v15, -2.0, s28
	ds_write_b16 v1, v4 offset:2352
	v_fma_f32 v4, v6, -2.0, s28
	v_subrev_f32_e32 v4, s29, v4
	v_mul_f32_e32 v4, 0x3fb8aa3b, v4
	v_exp_f32_e32 v4, v4
	v_cvt_f16_f32_e32 v2, v2
	v_subrev_f32_e32 v13, s29, v13
	v_subrev_f32_e32 v12, s29, v12
	v_cvt_f16_f32_e32 v4, v4
	ds_write_b16 v1, v2 offset:14112
	v_fma_f32 v2, v3, -2.0, s28
	v_subrev_f32_e32 v2, s29, v2
	ds_write_b16 v1, v4 offset:6272
	v_fma_f32 v4, v7, -2.0, s28
	v_subrev_f32_e32 v4, s29, v4
	v_mul_f32_e32 v4, 0x3fb8aa3b, v4
	v_exp_f32_e32 v4, v4
	v_mul_f32_e32 v13, 0x3fb8aa3b, v13
	v_mul_f32_e32 v12, 0x3fb8aa3b, v12
	v_mul_f32_e32 v2, 0x3fb8aa3b, v2
	v_cvt_f16_f32_e32 v4, v4
	v_exp_f32_e32 v13, v13
	v_exp_f32_e32 v12, v12
	v_exp_f32_e32 v2, v2
	ds_write_b16 v1, v4 offset:7056
	v_fma_f32 v4, v8, -2.0, s28
	v_subrev_f32_e32 v4, s29, v4
	v_mul_f32_e32 v4, 0x3fb8aa3b, v4
	v_exp_f32_e32 v4, v4
	v_cvt_f16_f32_e32 v13, v13
	v_cvt_f16_f32_e32 v12, v12
	v_cvt_f16_f32_e32 v2, v2
	v_cvt_f16_f32_e32 v4, v4
	ds_write_b16 v1, v13
	ds_write_b16 v1, v12 offset:784
	ds_write_b16 v1, v2 offset:14896
	ds_write_b16 v1, v4 offset:7840
	v_fma_f32 v4, v9, -2.0, s28
	v_subrev_f32_e32 v4, s29, v4
	v_mul_f32_e32 v4, 0x3fb8aa3b, v4
	v_exp_f32_e32 v4, v4
	s_nop 0
	v_cvt_f16_f32_e32 v4, v4
	ds_write_b16 v1, v4 offset:8624
	v_fma_f32 v4, v10, -2.0, s28
	v_subrev_f32_e32 v4, s29, v4
	v_mul_f32_e32 v4, 0x3fb8aa3b, v4
	v_exp_f32_e32 v4, v4
	s_nop 0
	v_cvt_f16_f32_e32 v4, v4
	ds_write_b16 v1, v4 offset:12544
	v_fma_f32 v4, v11, -2.0, s28
	v_subrev_f32_e32 v4, s29, v4
	v_mul_f32_e32 v4, 0x3fb8aa3b, v4
	v_exp_f32_e32 v4, v4
	s_nop 0
	v_cvt_f16_f32_e32 v4, v4
	ds_write_b16 v1, v4 offset:13328
	s_cmpk_gt_u32 s49, 0xff
	s_cbranch_scc1 .Lf_wo_done
	s_waitcnt vmcnt(0)
	v_cvt_f16_f32_e32 v100, v128
	v_cvt_f16_f32_e32 v103, v131
	v_cvt_pk_f16_f32 v101, v129, v130
	v_pack_b32_f16 v100, v100, v101
	v_alignbit_b32 v101, v103, v101, 16
	v_lshl_add_u64 v[104:105], v[132:133], 1, s[18:19]
	global_store_dwordx2 v[104:105], v[100:101], off
.Lf_wo_done:
.Lf_28:
	s_and_b32 s4, s51, 3
	s_cmpk_lt_u32 s49, 0x200
	s_waitcnt lgkmcnt(0)
	s_cselect_b64 s[2:3], -1, 0
	s_cmpk_gt_u32 s49, 0x1ff
	s_cbranch_scc1 .Lf_30
	s_lshl_b32 s5, s33, 6
	s_lshl_b32 s8, s4, 4
	s_load_dwordx2 s[6:7], s[0:1], 0x10
	s_or_b32 s5, s8, s5
	v_and_or_b32 v1, v0, 15, s5
	v_mul_u32_u24_e32 v1, 0x180, v1
	v_lshrrev_b32_e32 v2, 1, v0
	v_and_or_b32 v1, v2, 24, v1
	v_lshlrev_b32_e32 v1, 1, v1
	s_waitcnt lgkmcnt(0)
	global_load_dwordx4 v[46:49], v1, s[6:7]
	global_load_dwordx4 v[42:45], v1, s[6:7] offset:64
	global_load_dwordx4 v[38:41], v1, s[6:7] offset:128
	global_load_dwordx4 v[34:37], v1, s[6:7] offset:192
	global_load_dwordx4 v[30:33], v1, s[6:7] offset:256
	global_load_dwordx4 v[26:29], v1, s[6:7] offset:320
	global_load_dwordx4 v[22:25], v1, s[6:7] offset:384
	global_load_dwordx4 v[18:21], v1, s[6:7] offset:448
	global_load_dwordx4 v[14:17], v1, s[6:7] offset:512
	global_load_dwordx4 v[10:13], v1, s[6:7] offset:576
	global_load_dwordx4 v[6:9], v1, s[6:7] offset:640
	global_load_dwordx4 v[2:5], v1, s[6:7] offset:704

.Lattn_orig:
	s_load_dwordx2 s[4:5], s[0:1], 0x20
	s_movk_i32 s6, 0x100
	s_lshr_b32 s3, s2, 3
	v_readfirstlane_b32 s49, v0
	v_cmp_gt_u32_e32 vcc, s6, v0
	s_and_saveexec_b64 s[6:7], vcc
	s_cbranch_execz .LBB1_2
	s_lshl_b32 s12, s2, 5
	s_load_dwordx2 s[8:9], s[0:1], 0x28
	s_load_dwordx2 s[10:11], s[0:1], 0x38
	s_and_b32 s12, s12, 0xe0
	s_add_i32 s12, s12, s3
	s_mov_b32 s13, 0
	s_lshl_b64 s[12:13], s[12:13], 10
	v_lshl_or_b32 v6, v0, 2, s12
	v_mov_b32_e32 v7, s13
	s_waitcnt lgkmcnt(0)
	v_lshl_add_u64 v[2:3], v[6:7], 2, s[8:9]
	global_load_dwordx4 v[2:5], v[2:3], off
	s_waitcnt vmcnt(0)
	v_cvt_f16_f32_e32 v1, v2
	v_cvt_f16_f32_e32 v5, v5
	v_cvt_pk_f16_f32 v3, v3, v4
	v_pack_b32_f16 v2, v1, v3
	v_alignbit_b32 v3, v5, v3, 16
	v_lshl_add_u64 v[4:5], v[6:7], 1, s[10:11]
	global_store_dwordx2 v[4:5], v[2:3], off

	.amdhsa_kernel _Z11attn_kernelPKfS0_PKDF16_S0_S0_S0_S2_PDF16_S3_
		.amdhsa_group_segment_fixed_size 0
		.amdhsa_private_segment_fixed_size 0
		.amdhsa_kernarg_size 72
		.amdhsa_user_sgpr_count 2
		.amdhsa_user_sgpr_dispatch_ptr 0
		.amdhsa_user_sgpr_queue_ptr 0
		.amdhsa_user_sgpr_kernarg_segment_ptr 1
		.amdhsa_user_sgpr_dispatch_id 0
		.amdhsa_user_sgpr_kernarg_preload_length 0
		.amdhsa_user_sgpr_kernarg_preload_offset 0
		.amdhsa_user_sgpr_private_segment_size 0
		.amdhsa_uses_dynamic_stack 0
		.amdhsa_enable_private_segment 0
		.amdhsa_system_sgpr_workgroup_id_x 1
		.amdhsa_system_sgpr_workgroup_id_y 0
		.amdhsa_system_sgpr_workgroup_id_z 0
		.amdhsa_system_sgpr_workgroup_info 0
		.amdhsa_system_vgpr_workitem_id 0
		.amdhsa_next_free_vgpr 144
		.amdhsa_next_free_sgpr 64
		.amdhsa_accum_offset 144
		.amdhsa_reserve_vcc 1
		.amdhsa_float_round_mode_32 0
		.amdhsa_float_round_mode_16_64 0
		.amdhsa_float_denorm_mode_32 3
		.amdhsa_float_denorm_mode_16_64 3
		.amdhsa_dx10_clamp 1
		.amdhsa_ieee_mode 1
		.amdhsa_fp16_overflow 0
		.amdhsa_tg_split 0
		.amdhsa_exception_fp_ieee_invalid_op 0
		.amdhsa_exception_fp_denorm_src 0
		.amdhsa_exception_fp_ieee_div_zero 0
		.amdhsa_exception_fp_ieee_overflow 0
		.amdhsa_exception_fp_ieee_underflow 0
		.amdhsa_exception_fp_ieee_inexact 0
		.amdhsa_exception_int_div_zero 0
	.end_amdhsa_kernel

amdhsa.kernels:
  - .agpr_count:     0
    .args:
      - .actual_access:  read_only
        .address_space:  global
        .offset:         0
        .size:           8
        .value_kind:     global_buffer
      - .actual_access:  read_only
        .address_space:  global
        .offset:         8
        .size:           8
        .value_kind:     global_buffer
      - .actual_access:  read_only
        .address_space:  global
        .offset:         16
        .size:           8
        .value_kind:     global_buffer
      - .actual_access:  read_only
        .address_space:  global
        .offset:         24
        .size:           8
        .value_kind:     global_buffer
      - .address_space:  global
        .offset:         32
        .size:           8
        .value_kind:     global_buffer
      - .actual_access:  read_only
        .address_space:  global
        .offset:         40
        .size:           8
        .value_kind:     global_buffer
      - .address_space:  global
        .offset:         48
        .size:           8
        .value_kind:     global_buffer
      - .actual_access:  read_only
        .address_space:  global
        .offset:         56
        .size:           8
        .value_kind:     global_buffer
      - .address_space:  global
        .offset:         64
        .size:           8
        .value_kind:     global_buffer
      - .address_space:  global
        .offset:         72
        .size:           8
        .value_kind:     global_buffer
      - .address_space:  global
        .offset:         80
        .size:           8
        .value_kind:     global_buffer
      - .address_space:  global
        .offset:         88
        .size:           8
        .value_kind:     global_buffer
      - .address_space:  global
        .offset:         96
        .size:           8
        .value_kind:     global_buffer
      - .actual_access:  write_only
        .address_space:  global
        .offset:         104
        .size:           8
        .value_kind:     global_buffer
      - .actual_access:  write_only
        .address_space:  global
        .offset:         112
        .size:           8
        .value_kind:     global_buffer
      - .actual_access:  write_only
        .address_space:  global
        .offset:         120
        .size:           8
        .value_kind:     global_buffer
      - .actual_access:  write_only
        .address_space:  global
        .offset:         128
        .size:           8
        .value_kind:     global_buffer
      - .address_space:  global
        .offset:         136
        .size:           8
        .value_kind:     global_buffer
      - .address_space:  global
        .offset:         144
        .size:           8
        .value_kind:     global_buffer
      - .actual_access:  write_only
        .address_space:  global
        .offset:         152
        .size:           8
        .value_kind:     global_buffer
    .group_segment_fixed_size: 46112
    .kernarg_segment_align: 8
    .kernarg_segment_size: 160
    .language:       OpenCL C
    .language_version:
      - 2
      - 0
    .max_flat_workgroup_size: 512
    .name:           _Z11proj_kernelPKfS0_S0_S0_S0_S0_S0_S0_S0_S0_S0_S0_S0_PfS1_PDF16_S1_S0_S0_S2_
    .private_segment_fixed_size: 0
    .sgpr_count:     33
    .sgpr_spill_count: 0
    .symbol:         _Z11proj_kernelPKfS0_S0_S0_S0_S0_S0_S0_S0_S0_S0_S0_S0_PfS1_PDF16_S1_S0_S0_S2_.kd
    .uniform_work_group_size: 1
    .uses_dynamic_stack: false
    .vgpr_count:     133
    .vgpr_spill_count: 0
    .wavefront_size: 64
  - .agpr_count:     0
    .args:
      - .actual_access:  read_only
        .address_space:  global
        .offset:         0
        .size:           8
        .value_kind:     global_buffer
      - .actual_access:  read_only
        .address_space:  global
        .offset:         8
        .size:           8
        .value_kind:     global_buffer
      - .actual_access:  read_only
        .address_space:  global
        .offset:         16
        .size:           8
        .value_kind:     global_buffer
      - .actual_access:  read_only
        .address_space:  global
        .offset:         24
        .size:           8
        .value_kind:     global_buffer
      - .actual_access:  read_only
        .address_space:  global
        .offset:         32
        .size:           8
        .value_kind:     global_buffer
      - .actual_access:  read_only
        .address_space:  global
        .offset:         40
        .size:           8
        .value_kind:     global_buffer
      - .actual_access:  read_only
        .address_space:  global
        .offset:         48
        .size:           8
        .value_kind:     global_buffer
      - .actual_access:  write_only
        .address_space:  global
        .offset:         56
        .size:           8
        .value_kind:     global_buffer
      - .actual_access:  write_only
        .address_space:  global
        .offset:         64
        .size:           8
        .value_kind:     global_buffer
    .group_segment_fixed_size: 0
    .kernarg_segment_align: 8
    .kernarg_segment_size: 72
    .language:       OpenCL C
    .language_version:
      - 2
      - 0
    .max_flat_workgroup_size: 768
    .name:           _Z11attn_kernelPKfS0_PKDF16_S0_S0_S0_S2_PDF16_S3_
    .private_segment_fixed_size: 0
    .sgpr_count:     70
    .sgpr_spill_count: 0
    .symbol:         _Z11attn_kernelPKfS0_PKDF16_S0_S0_S0_S2_PDF16_S3_.kd
    .uniform_work_group_size: 1
    .uses_dynamic_stack: false
    .vgpr_count:     144
    .vgpr_spill_count: 0
    .wavefront_size: 64
  - .agpr_count:     8
    .args:
      - .actual_access:  read_only
        .address_space:  global
        .offset:         0
        .size:           8
        .value_kind:     global_buffer
      - .actual_access:  read_only
        .address_space:  global
        .offset:         8
        .size:           8
        .value_kind:     global_buffer
      - .actual_access:  read_only
        .address_space:  global
        .offset:         16
        .size:           8
        .value_kind:     global_buffer
      - .actual_access:  write_only
        .address_space:  global
        .offset:         24
        .size:           8
        .value_kind:     global_buffer
    .group_segment_fixed_size: 27648
    .kernarg_segment_align: 8
    .kernarg_segment_size: 32
    .language:       OpenCL C
    .language_version:
      - 2
      - 0
    .max_flat_workgroup_size: 256
    .name:           _Z10out_kernelPKDF16_S0_PKfPf
    .private_segment_fixed_size: 0
    .sgpr_count:     18
    .sgpr_spill_count: 0
    .symbol:         _Z10out_kernelPKDF16_S0_PKfPf.kd
    .uniform_work_group_size: 1
    .uses_dynamic_stack: false
    .vgpr_count:     88
    .vgpr_spill_count: 0
    .wavefront_size: 64
